# speedup vs baseline: 1.0088x; 1.0088x over previous
.Llight_path:
	s_waitcnt vmcnt(16)
	v_mul_u32_u24_e32 v236, 36, v228
	v_add_u32_e32 v236, v236, v230
	v_add_u32_e32 v237, s7, v229
	v_mul_u32_u24_e32 v238, 0x104, v228
	v_add_u32_e32 v238, v238, v237
	v_add_u32_e32 v238, 0xb840, v238
	v_add_u32_e32 v231, s7, v229
	v_add_u32_e32 v231, 0xb840, v231
	v_add_u32_e32 v211, s6, v210
	s_nop 0
	s_load_dwordx8 s[4:11], s[0:1], 0x10
	v_add_u32_e32 v232, 0x24e80, v228
	ds_read_b32 v244, v232
	ds_read_b32 v245, v232 offset:128
	ds_read_b128 v[2:5], v237 offset:36928
	ds_read_b128 v[6:9], v237 offset:36944
	ds_read_b128 v[10:13], v237 offset:36960
	ds_read_b128 v[14:17], v237 offset:36976
	ds_read_b128 v[18:21], v237 offset:37056
	ds_read_b128 v[22:25], v237 offset:37072
	ds_read_b128 v[26:29], v237 offset:37088
	ds_read_b128 v[30:33], v237 offset:37104
	ds_read_b128 v[162:165], v236 offset:16384
	ds_read_b128 v[166:169], v236 offset:16416
	ds_read_b128 v[170:173], v236 offset:16448
	ds_read_b128 v[174:177], v236 offset:16480
	s_waitcnt lgkmcnt(0)
	v_mfma_f32_32x32x16_bf16 v[2:17], v[94:97], v[162:165], v[2:17]
	v_mfma_f32_32x32x16_bf16 v[2:17], v[90:93], v[166:169], v[2:17]
	v_mfma_f32_32x32x16_bf16 v[2:17], v[86:89], v[170:173], v[2:17]
	v_mfma_f32_32x32x16_bf16 v[2:17], v[82:85], v[174:177], v[2:17]
	v_mfma_f32_32x32x16_bf16 v[18:33], v[46:49], v[162:165], v[18:33]
	ds_read_b128 v[130:133], v237 offset:36928
	ds_read_b128 v[134:137], v237 offset:36944
	ds_read_b128 v[138:141], v237 offset:36960
	v_mfma_f32_32x32x16_bf16 v[18:33], v[42:45], v[166:169], v[18:33]
	ds_read_b128 v[142:145], v237 offset:36976
	ds_read_b128 v[146:149], v237 offset:37056
	ds_read_b128 v[150:153], v237 offset:37072
	v_mfma_f32_32x32x16_bf16 v[18:33], v[38:41], v[170:173], v[18:33]
	ds_read_b128 v[154:157], v237 offset:37088
	ds_read_b128 v[158:161], v237 offset:37104
	ds_read_b128 v[178:181], v236 offset:20992
	v_mfma_f32_32x32x16_bf16 v[18:33], v[34:37], v[174:177], v[18:33]
	ds_read_b128 v[182:185], v236 offset:21024
	ds_read_b128 v[186:189], v236 offset:21056
	ds_read_b128 v[190:193], v236 offset:21088
	s_waitcnt lgkmcnt(0)
	v_mfma_f32_32x32x16_bf16 v[130:145], v[94:97], v[178:181], v[130:145]
	v_mfma_f32_32x32x16_bf16 v[130:145], v[90:93], v[182:185], v[130:145]
	v_mfma_f32_32x32x16_bf16 v[130:145], v[86:89], v[186:189], v[130:145]
	v_mfma_f32_32x32x16_bf16 v[130:145], v[82:85], v[190:193], v[130:145]
	s_nop 7
	ds_write_b128 v238, v[2:5] offset:0
	ds_write_b128 v238, v[6:9] offset:16
	ds_write_b128 v238, v[10:13] offset:32
	ds_write_b128 v238, v[14:17] offset:48
	ds_write_b128 v238, v[18:21] offset:128
	ds_write_b128 v238, v[22:25] offset:144
	ds_write_b128 v238, v[26:29] offset:160
	ds_write_b128 v238, v[30:33] offset:176
	v_mfma_f32_32x32x16_bf16 v[146:161], v[46:49], v[178:181], v[146:161]
	ds_read_b128 v[2:5], v237 offset:36928
	ds_read_b128 v[6:9], v237 offset:36944
	ds_read_b128 v[10:13], v237 offset:36960
	v_mfma_f32_32x32x16_bf16 v[146:161], v[42:45], v[182:185], v[146:161]
	ds_read_b128 v[14:17], v237 offset:36976
	ds_read_b128 v[18:21], v237 offset:37056
	ds_read_b128 v[22:25], v237 offset:37072
	v_mfma_f32_32x32x16_bf16 v[146:161], v[38:41], v[186:189], v[146:161]
	ds_read_b128 v[26:29], v237 offset:37088
	ds_read_b128 v[30:33], v237 offset:37104
	ds_read_b128 v[162:165], v236 offset:25600
	v_mfma_f32_32x32x16_bf16 v[146:161], v[34:37], v[190:193], v[146:161]
	ds_read_b128 v[166:169], v236 offset:25632
	ds_read_b128 v[170:173], v236 offset:25664
	ds_read_b128 v[174:177], v236 offset:25696
	s_waitcnt lgkmcnt(0)
	v_mfma_f32_32x32x16_bf16 v[2:17], v[94:97], v[162:165], v[2:17]
	v_mfma_f32_32x32x16_bf16 v[2:17], v[90:93], v[166:169], v[2:17]
	v_mfma_f32_32x32x16_bf16 v[2:17], v[86:89], v[170:173], v[2:17]
	v_mfma_f32_32x32x16_bf16 v[2:17], v[82:85], v[174:177], v[2:17]
	s_nop 7
	v_add_u32_e32 v239, 0x8200, v238
	ds_write_b128 v239, v[130:133] offset:0
	ds_write_b128 v239, v[134:137] offset:16
	ds_write_b128 v239, v[138:141] offset:32
	ds_write_b128 v239, v[142:145] offset:48
	ds_write_b128 v239, v[146:149] offset:128
	ds_write_b128 v239, v[150:153] offset:144
	ds_write_b128 v239, v[154:157] offset:160
	ds_write_b128 v239, v[158:161] offset:176
	v_mfma_f32_32x32x16_bf16 v[18:33], v[46:49], v[162:165], v[18:33]
	ds_read_b128 v[130:133], v237 offset:36928
	ds_read_b128 v[134:137], v237 offset:36944
	ds_read_b128 v[138:141], v237 offset:36960
	v_mfma_f32_32x32x16_bf16 v[18:33], v[42:45], v[166:169], v[18:33]
	ds_read_b128 v[142:145], v237 offset:36976
	ds_read_b128 v[146:149], v237 offset:37056
	ds_read_b128 v[150:153], v237 offset:37072
	v_mfma_f32_32x32x16_bf16 v[18:33], v[38:41], v[170:173], v[18:33]
	ds_read_b128 v[154:157], v237 offset:37088
	ds_read_b128 v[158:161], v237 offset:37104
	ds_read_b128 v[178:181], v236 offset:30208
	v_mfma_f32_32x32x16_bf16 v[18:33], v[34:37], v[174:177], v[18:33]
	ds_read_b128 v[182:185], v236 offset:30240
	ds_read_b128 v[186:189], v236 offset:30272
	ds_read_b128 v[190:193], v236 offset:30304
	s_waitcnt lgkmcnt(0)
	v_mfma_f32_32x32x16_bf16 v[130:145], v[94:97], v[178:181], v[130:145]
	v_mfma_f32_32x32x16_bf16 v[130:145], v[90:93], v[182:185], v[130:145]
	v_mfma_f32_32x32x16_bf16 v[130:145], v[86:89], v[186:189], v[130:145]
	v_mfma_f32_32x32x16_bf16 v[130:145], v[82:85], v[190:193], v[130:145]
	s_nop 7
	v_add_u32_e32 v239, 0x10400, v238
	ds_write_b128 v239, v[2:5] offset:0
	ds_write_b128 v239, v[6:9] offset:16
	ds_write_b128 v239, v[10:13] offset:32
	ds_write_b128 v239, v[14:17] offset:48
	ds_write_b128 v239, v[18:21] offset:128
	ds_write_b128 v239, v[22:25] offset:144
	ds_write_b128 v239, v[26:29] offset:160
	ds_write_b128 v239, v[30:33] offset:176
	v_mfma_f32_32x32x16_bf16 v[146:161], v[46:49], v[178:181], v[146:161]
	v_mfma_f32_32x32x16_bf16 v[146:161], v[42:45], v[182:185], v[146:161]
	v_mfma_f32_32x32x16_bf16 v[146:161], v[38:41], v[186:189], v[146:161]
	v_mfma_f32_32x32x16_bf16 v[146:161], v[34:37], v[190:193], v[146:161]
	s_nop 7
	s_nop 7
	v_cmp_gt_u32_e32 vcc, 16, v228
	s_and_saveexec_b64 s[20:21], vcc
	v_add_u32_e32 v239, 0x18600, v238
	ds_write_b128 v239, v[130:133] offset:0
	ds_write_b128 v239, v[134:137] offset:16
	ds_write_b128 v239, v[138:141] offset:32
	ds_write_b128 v239, v[142:145] offset:48
	ds_write_b128 v239, v[146:149] offset:128
	ds_write_b128 v239, v[150:153] offset:144
	ds_write_b128 v239, v[154:157] offset:160
	ds_write_b128 v239, v[158:161] offset:176
	s_or_b64 exec, exec, s[20:21]
	s_mov_b32 s12, 0xbeb17218
	v_mov_b32_e32 v235, 0xc038aa3b
	v_add_u32_e32 v233, v231, v244
	v_add_u32_e32 v234, v231, v245
	ds_read_b128 v[2:5], v233 offset:0
	ds_read_b128 v[6:9], v233 offset:16
	ds_read_b128 v[10:13], v233 offset:32
	ds_read_b128 v[14:17], v233 offset:48
	ds_read_b128 v[18:21], v233 offset:128
	ds_read_b128 v[22:25], v233 offset:144
	ds_read_b128 v[26:29], v233 offset:160
	ds_read_b128 v[30:33], v233 offset:176
	ds_read_b128 v[34:37], v234 offset:0
	ds_read_b128 v[38:41], v234 offset:16
	ds_read_b128 v[42:45], v234 offset:32
	ds_read_b128 v[46:49], v234 offset:48
	v_mov_b32_e32 v194, 0
	v_mov_b32_e32 v195, 0
	v_mov_b32_e32 v196, 0
	v_mov_b32_e32 v197, 0
	v_mov_b32_e32 v198, 0
	v_mov_b32_e32 v199, 0
	v_mov_b32_e32 v200, 0
	v_mov_b32_e32 v201, 0
	v_mov_b32_e32 v202, 0
	v_mov_b32_e32 v203, 0
	v_mov_b32_e32 v204, 0
	v_mov_b32_e32 v205, 0
	v_mov_b32_e32 v206, 0
	v_mov_b32_e32 v207, 0
	v_mov_b32_e32 v208, 0
	v_mov_b32_e32 v209, 0
	v_add_u32_e32 v232, 0x100, v232
	s_movk_i32 s16, 18
	s_waitcnt vmcnt(0) lgkmcnt(0)
	ds_read_b128 v[82:85], v234 offset:128
	ds_read_b128 v[86:89], v234 offset:144
	ds_read_b128 v[90:93], v234 offset:160
	ds_read_b128 v[94:97], v234 offset:176
	ds_read2_b32 v[244:245], v232 offset1:32
	v_exp_f32_e32 v212, v4
	v_exp_f32_e32 v213, v8
	v_exp_f32_e32 v214, v12
	v_exp_f32_e32 v215, v16
	v_exp_f32_e32 v217, v2
	v_fma_f32 v251, v212, s12, s12
	v_exp_f32_e32 v218, v6
	v_fma_f32 v252, v213, s12, s12
	v_exp_f32_e32 v219, v10
	v_fma_f32 v253, v214, s12, s12
	v_exp_f32_e32 v220, v14
	v_fma_f32 v254, v215, s12, s12
	v_fmac_f32_e32 v251, v217, v251
	v_fmac_f32_e32 v252, v218, v252
	v_fmac_f32_e32 v253, v219, v253
	v_fmac_f32_e32 v254, v220, v254
	v_rcp_f32_e32 v217, v251
	v_rcp_f32_e32 v218, v252
	v_rcp_f32_e32 v219, v253
	v_rcp_f32_e32 v220, v254
	v_exp_f32_e32 v246, v5
	v_fma_f32 v194, -v212, v217, v217
	v_exp_f32_e32 v247, v9
	v_fma_f32 v195, -v213, v218, v218
	v_exp_f32_e32 v248, v13
	v_fma_f32 v196, -v214, v219, v219
	v_exp_f32_e32 v249, v17
	v_fma_f32 v197, -v215, v220, v220
	v_exp_f32_e32 v212, v194
	v_add_f32_e32 v246, 1.0, v246
	v_exp_f32_e32 v213, v195
	v_add_f32_e32 v247, 1.0, v247
	v_exp_f32_e32 v214, v196
	v_add_f32_e32 v248, 1.0, v248
	v_exp_f32_e32 v215, v197
	v_add_f32_e32 v249, 1.0, v249
	v_fmac_f32_e32 v246, v246, v212
	v_fmac_f32_e32 v247, v247, v213
	v_fmac_f32_e32 v248, v248, v214
	v_fmac_f32_e32 v249, v249, v215
	v_rcp_f32_e32 v246, v246
	v_rcp_f32_e32 v247, v247
	v_rcp_f32_e32 v248, v248
	v_rcp_f32_e32 v249, v249
	v_fma_f32 v246, -v212, v246, v246
	v_fma_f32 v247, -v213, v247, v247
	v_fma_f32 v248, -v214, v248, v248
	v_fma_f32 v249, -v215, v249, v249
	v_cvt_pk_bf16_f32 v236, v246, v247
	v_cvt_pk_bf16_f32 v237, v248, v249
	s_waitcnt lgkmcnt(0)
	v_add_u32_e32 v233, v231, v244
	ds_read_b128 v[2:5], v233 offset:0
	ds_read_b128 v[6:9], v233 offset:16
	ds_read_b128 v[10:13], v233 offset:32
	ds_read_b128 v[14:17], v233 offset:48
	v_exp_f32_e32 v212, v20
	v_exp_f32_e32 v213, v24
	v_exp_f32_e32 v214, v28
	v_exp_f32_e32 v215, v32
	v_exp_f32_e32 v217, v18
	v_fma_f32 v251, v212, s12, s12
	v_exp_f32_e32 v218, v22
	v_fma_f32 v252, v213, s12, s12
	v_exp_f32_e32 v219, v26
	v_fma_f32 v253, v214, s12, s12
	v_exp_f32_e32 v220, v30
	v_fma_f32 v254, v215, s12, s12
	v_fmac_f32_e32 v251, v217, v251
	v_fmac_f32_e32 v252, v218, v252
	v_fmac_f32_e32 v253, v219, v253
	v_fmac_f32_e32 v254, v220, v254
	v_rcp_f32_e32 v217, v251
	v_rcp_f32_e32 v218, v252
	v_rcp_f32_e32 v219, v253
	v_rcp_f32_e32 v220, v254
	v_exp_f32_e32 v246, v21
	v_fma_f32 v198, -v212, v217, v217
	v_exp_f32_e32 v247, v25
	v_fma_f32 v199, -v213, v218, v218
	v_exp_f32_e32 v248, v29
	v_fma_f32 v200, -v214, v219, v219
	v_exp_f32_e32 v249, v33
	v_fma_f32 v201, -v215, v220, v220
	v_exp_f32_e32 v212, v198
	v_add_f32_e32 v246, 1.0, v246
	v_exp_f32_e32 v213, v199
	v_add_f32_e32 v247, 1.0, v247
	v_exp_f32_e32 v214, v200
	v_add_f32_e32 v248, 1.0, v248
	v_exp_f32_e32 v215, v201
	v_add_f32_e32 v249, 1.0, v249
	v_fmac_f32_e32 v246, v246, v212
	v_fmac_f32_e32 v247, v247, v213
	v_fmac_f32_e32 v248, v248, v214
	v_fmac_f32_e32 v249, v249, v215
	v_rcp_f32_e32 v246, v246
	v_rcp_f32_e32 v247, v247
	v_rcp_f32_e32 v248, v248
	v_rcp_f32_e32 v249, v249
	v_fma_f32 v246, -v212, v246, v246
	v_fma_f32 v247, -v213, v247, v247
	v_fma_f32 v248, -v214, v248, v248
	v_fma_f32 v249, -v215, v249, v249
	v_cvt_pk_bf16_f32 v238, v246, v247
	v_cvt_pk_bf16_f32 v239, v248, v249
	ds_write_b128 v211, v[236:239] offset:0
	s_waitcnt lgkmcnt(0)
	s_barrier
	ds_read_b128 v[130:133], v210 offset:0
	ds_read_b128 v[134:137], v210 offset:1024
	ds_read_b128 v[18:21], v233 offset:128
	ds_read_b128 v[22:25], v233 offset:144
	ds_read_b128 v[26:29], v233 offset:160
	ds_read_b128 v[30:33], v233 offset:176
	v_exp_f32_e32 v212, v36
	v_exp_f32_e32 v213, v40
	v_exp_f32_e32 v214, v44
	v_exp_f32_e32 v215, v48
	ds_read_b128 v[138:141], v210 offset:2048
	ds_read_b128 v[142:145], v210 offset:3072
	v_exp_f32_e32 v217, v34
	v_fma_f32 v251, v212, s12, s12
	v_exp_f32_e32 v218, v38
	v_fma_f32 v252, v213, s12, s12
	v_exp_f32_e32 v219, v42
	v_fma_f32 v253, v214, s12, s12
	v_exp_f32_e32 v220, v46
	v_fma_f32 v254, v215, s12, s12
	ds_read_b128 v[146:149], v210 offset:4096
	ds_read_b128 v[150:153], v210 offset:5120
	v_fmac_f32_e32 v251, v217, v251
	v_fmac_f32_e32 v252, v218, v252
	v_fmac_f32_e32 v253, v219, v253
	v_fmac_f32_e32 v254, v220, v254
	ds_read_b128 v[154:157], v210 offset:6144
	ds_read_b128 v[158:161], v210 offset:7168
	v_rcp_f32_e32 v217, v251
	v_rcp_f32_e32 v218, v252
	v_rcp_f32_e32 v219, v253
	v_rcp_f32_e32 v220, v254
	v_exp_f32_e32 v246, v37
	v_fma_f32 v202, -v212, v217, v217
	v_exp_f32_e32 v247, v41
	v_fma_f32 v203, -v213, v218, v218
	v_exp_f32_e32 v248, v45
	v_fma_f32 v204, -v214, v219, v219
	v_exp_f32_e32 v249, v49
	v_fma_f32 v205, -v215, v220, v220
	v_exp_f32_e32 v212, v202
	v_add_f32_e32 v246, 1.0, v246
	v_exp_f32_e32 v213, v203
	v_add_f32_e32 v247, 1.0, v247
	v_exp_f32_e32 v214, v204
	v_add_f32_e32 v248, 1.0, v248
	v_exp_f32_e32 v215, v205
	v_add_f32_e32 v249, 1.0, v249
	v_fmac_f32_e32 v246, v246, v212
	v_fmac_f32_e32 v247, v247, v213
	v_fmac_f32_e32 v248, v248, v214
	v_fmac_f32_e32 v249, v249, v215
	v_rcp_f32_e32 v246, v246
	v_rcp_f32_e32 v247, v247
	v_rcp_f32_e32 v248, v248
	v_rcp_f32_e32 v249, v249
	v_fma_f32 v246, -v212, v246, v246
	v_fma_f32 v247, -v213, v247, v247
	v_fma_f32 v248, -v214, v248, v248
	v_fma_f32 v249, -v215, v249, v249
	v_cvt_pk_bf16_f32 v236, v246, v247
	v_cvt_pk_bf16_f32 v237, v248, v249
	s_waitcnt lgkmcnt(0)
	v_mfma_f32_32x32x16_bf16 v[2:17], v[126:129], v[130:133], v[2:17]
	v_add_u32_e32 v234, v231, v245
	ds_read_b128 v[34:37], v234 offset:0
	ds_read_b128 v[38:41], v234 offset:16
	ds_read_b128 v[42:45], v234 offset:32
	ds_read_b128 v[46:49], v234 offset:48
	v_add_u32_e32 v232, 0x100, v232
	v_exp_f32_e32 v212, v84
	v_exp_f32_e32 v213, v88
	v_exp_f32_e32 v214, v92
	v_exp_f32_e32 v215, v96
	v_mfma_f32_32x32x16_bf16 v[2:17], v[122:125], v[134:137], v[2:17]
	v_exp_f32_e32 v217, v82
	v_fma_f32 v251, v212, s12, s12
	v_exp_f32_e32 v218, v86
	v_fma_f32 v252, v213, s12, s12
	v_exp_f32_e32 v219, v90
	v_fma_f32 v253, v214, s12, s12
	v_exp_f32_e32 v220, v94
	v_fma_f32 v254, v215, s12, s12
	v_mfma_f32_32x32x16_bf16 v[2:17], v[118:121], v[138:141], v[2:17]
	v_fmac_f32_e32 v251, v217, v251
	v_fmac_f32_e32 v252, v218, v252
	v_fmac_f32_e32 v253, v219, v253
	v_fmac_f32_e32 v254, v220, v254
	v_mfma_f32_32x32x16_bf16 v[2:17], v[114:117], v[142:145], v[2:17]
	v_rcp_f32_e32 v217, v251
	v_rcp_f32_e32 v218, v252
	v_rcp_f32_e32 v219, v253
	v_rcp_f32_e32 v220, v254
	v_mfma_f32_32x32x16_bf16 v[2:17], v[110:113], v[146:149], v[2:17]
	v_exp_f32_e32 v246, v85
	v_fma_f32 v206, -v212, v217, v217
	v_exp_f32_e32 v247, v89
	v_fma_f32 v207, -v213, v218, v218
	v_exp_f32_e32 v248, v93
	v_fma_f32 v208, -v214, v219, v219
	v_exp_f32_e32 v249, v97
	v_fma_f32 v209, -v215, v220, v220
	v_mfma_f32_32x32x16_bf16 v[2:17], v[106:109], v[150:153], v[2:17]
	v_mfma_f32_32x32x16_bf16 v[2:17], v[102:105], v[154:157], v[2:17]
	v_exp_f32_e32 v212, v206
	v_add_f32_e32 v246, 1.0, v246
	v_exp_f32_e32 v213, v207
	v_add_f32_e32 v247, 1.0, v247
	v_exp_f32_e32 v214, v208
	v_add_f32_e32 v248, 1.0, v248
	v_exp_f32_e32 v215, v209
	v_add_f32_e32 v249, 1.0, v249
	v_fmac_f32_e32 v246, v246, v212
	v_fmac_f32_e32 v247, v247, v213
	v_fmac_f32_e32 v248, v248, v214
	v_fmac_f32_e32 v249, v249, v215
	v_mfma_f32_32x32x16_bf16 v[2:17], v[98:101], v[158:161], v[2:17]
	v_rcp_f32_e32 v246, v246
	v_rcp_f32_e32 v247, v247
	v_rcp_f32_e32 v248, v248
	v_rcp_f32_e32 v249, v249
	v_fma_f32 v246, -v212, v246, v246
	v_fma_f32 v247, -v213, v247, v247
	v_fma_f32 v248, -v214, v248, v248
	v_fma_f32 v249, -v215, v249, v249
	v_cvt_pk_bf16_f32 v238, v246, v247
	v_cvt_pk_bf16_f32 v239, v248, v249
	ds_write_b128 v211, v[236:239] offset:8192
	s_waitcnt lgkmcnt(0)
	s_barrier
	.p2align 6
